# MoBA near-diagonal tiles: 32 clamped bias reads issued together behind one wait instead of 16 exec-masked reads each with its own wait
# speedup vs baseline: 1.0059x; 1.0044x over previous
; template <bool MLA>
; __device__ __forceinline__ void attn_unit(char* lds, int h, int qb, const bf16_t* Qp, int ldq, const bf16_t* Kp, int ldk, const bf16_t* KRp, const bf16_t* Vp, int ldv,
;                                           unsigned char* Op, int ldo, const float* KMp, const float* rel_bias) {
;     ...
;         if (MLA || jb == qb) act = (kb <= qlo + 31) ? 1 : 0; else act = __any((int)((mysel >> jb) & 1u)) ? 1 : 0;
;         act = __builtin_amdgcn_readfirstlane(act);
;         if (act) {
;             f32x16 p0, p1;
; #pragma unroll
;             for (int r = 0; r < 16; ++r) { p0[r] = 0.f; p1[r] = 0.f; }
;             { const char* kn = lds + buf * SHM_KN; const char* kr = lds + buf * SHM_KR;
; #pragma unroll
;               for (int d0 = 0; d0 < 8; ++d0) { const char* ap = kn + kan[d0 & 3] + (d0 >> 2) * 128;
;                   const bf16x8 a0 = *(const bf16x8*)ap, a1 = *(const bf16x8*)(ap + 32 * 256);
;                   p0 = __builtin_amdgcn_mfma_f32_32x32x16_bf16(a0, qr[d0], p0, 0, 0, 0);
;                   p1 = __builtin_amdgcn_mfma_f32_32x32x16_bf16(a1, qr[d0], p1, 0, 0, 0); }
;               if constexpr (MLA) {
; #pragma unroll
;                   for (int d0 = 8; d0 < 12; ++d0) { const char* ap = kr + kar[d0 & 3];
;                       const bf16x8 a0 = *(const bf16x8*)ap, a1 = *(const bf16x8*)(ap + 32 * 128);
;                       p0 = __builtin_amdgcn_mfma_f32_32x32x16_bf16(a0, qr[d0], p0, 0, 0, 0);
;                       p1 = __builtin_amdgcn_mfma_f32_32x32x16_bf16(a1, qr[d0], p1, 0, 0, 0); } } }
;             const int dq = qpos - kb - 4 * hi;
;             if constexpr (MLA) {
;                 if (kb + 63 > qlo) {
; #pragma unroll
;                     for (int r = 0; r < 16; ++r) { const int d0 = dq - CROWC(r); if (d0 < 0) p0[r] = NEG; if (d0 < 32) p1[r] = NEG; } }
;             } else {
;                 const bool selq = (jb == qb) || (((mysel >> jb) & 1u) != 0u);
;                 if (q0 - (kb + 63) >= 128) { const float cb = bt_l[128];
; #pragma unroll
;                     for (int r = 0; r < 16; ++r) { p0[r] = selq ? p0[r] + cb : NEG; p1[r] = selq ? p1[r] + cb : NEG; } }
;                 else {
; #pragma unroll
;                     for (int r4 = 0; r4 < 4; ++r4) {
; #pragma unroll
;                         for (int rr = 0; rr < 4; ++rr) { const int r = r4 * 4 + rr; const int d0 = dq - CROWC(r), d1 = d0 - 32;
.LBB0_1559:
	v_cndmask_b32_e64 v2, 0, 1, s[54:55]
	s_nop 0
	v_readfirstlane_b32 s22, v2
	s_bitcmp0_b32 s22, 0
	s_cbranch_scc1 .Lmoba_inact
	s_add_i32 s22, s75, 0
	v_add_u32_e32 v2, s22, v203
	ds_read_b128 v[68:71], v2 offset:32768
	ds_read_b128 v[72:75], v2 offset:32896
	s_mov_b64 s[54:55], -1
	s_waitcnt lgkmcnt(0)
	v_mfma_f32_32x32x16_bf16 v[100:115], v[68:71], v[160:163], 0
	s_xor_b32 s100, s75, 0x4000
	s_add_i32 s100, s27, s100
	v_lshl_add_u64 v[228:229], s[52:53], 0, v[182:183]
	s_add_i32 m0, s100, 0x8000
	s_nop 0
	global_load_lds_dwordx4 v[228:229], off
	ds_read_b128 v[68:71], v2 offset:40960
	ds_read_b128 v[76:79], v2 offset:41088
	v_add_u32_e32 v2, s22, v204
	s_waitcnt lgkmcnt(0)
	v_mfma_f32_32x32x16_bf16 v[84:99], v[68:71], v[160:163], 0
	v_lshl_add_u64 v[228:229], s[52:53], 0, v[180:181]
	v_lshl_add_u64 v[230:231], v[228:229], 0, s[46:47]
	s_mov_b32 m0, s100
	v_lshl_add_u64 v[228:229], v[228:229], 0, s[48:49]
	global_load_lds_dwordx4 v[230:231], off
	ds_read_b128 v[68:71], v2 offset:32768
	ds_read_b128 v[80:83], v2 offset:32896
	s_waitcnt lgkmcnt(0)
	v_mfma_f32_32x32x16_bf16 v[100:115], v[68:71], v[156:159], v[100:115]
	v_lshl_add_u64 v[230:231], s[52:53], 0, v[184:185]
	s_add_i32 m0, s100, 0x8400
	s_nop 0
	global_load_lds_dwordx4 v[230:231], off
	ds_read_b128 v[68:71], v2 offset:40960
	ds_read_b128 v[116:119], v2 offset:41088
	v_add_u32_e32 v2, s22, v205
	s_waitcnt lgkmcnt(0)
	v_mfma_f32_32x32x16_bf16 v[84:99], v[68:71], v[156:159], v[84:99]
	s_add_i32 m0, s100, 0x400
	s_nop 0
	global_load_lds_dwordx4 v[228:229], off
	ds_read_b128 v[68:71], v2 offset:32768
	ds_read_b128 v[120:123], v2 offset:32896
	s_waitcnt lgkmcnt(0)
	v_mfma_f32_32x32x16_bf16 v[100:115], v[68:71], v[152:155], v[100:115]
	ds_read_b128 v[68:71], v2 offset:40960
	ds_read_b128 v[124:127], v2 offset:41088
	v_add_u32_e32 v2, s22, v206
	s_lshl_b32 s22, 1, s76
	s_waitcnt lgkmcnt(0)
	v_mfma_f32_32x32x16_bf16 v[84:99], v[68:71], v[152:155], v[84:99]
	ds_read_b128 v[68:71], v2 offset:32768
	ds_read_b128 v[128:131], v2 offset:32896
	s_waitcnt lgkmcnt(0)
	v_mfma_f32_32x32x16_bf16 v[100:115], v[68:71], v[148:151], v[100:115]
	ds_read_b128 v[68:71], v2 offset:40960
	ds_read_b128 v[222:225], v2 offset:41088
	v_and_b32_e32 v2, s22, v219
	v_cmp_ne_u32_e32 vcc, 0, v2
	s_or_b64 s[12:13], s[12:13], vcc
	s_cmpk_gt_i32 s69, 0x7f
	s_waitcnt lgkmcnt(0)
	v_mfma_f32_32x32x16_bf16 v[84:99], v[68:71], v[148:151], v[84:99]
	v_mfma_f32_32x32x16_bf16 v[100:115], v[72:75], v[144:147], v[100:115]
	v_mfma_f32_32x32x16_bf16 v[84:99], v[76:79], v[144:147], v[84:99]
	v_mfma_f32_32x32x16_bf16 v[100:115], v[80:83], v[140:143], v[100:115]
	v_mfma_f32_32x32x16_bf16 v[84:99], v[116:119], v[140:143], v[84:99]
	v_mfma_f32_32x32x16_bf16 v[100:115], v[120:123], v[136:139], v[100:115]
	v_mfma_f32_32x32x16_bf16 v[84:99], v[124:127], v[136:139], v[84:99]
	v_mfma_f32_32x32x16_bf16 v[100:115], v[128:131], v[132:135], v[100:115]
	v_mfma_f32_32x32x16_bf16 v[84:99], v[222:225], v[132:135], v[84:99]
	s_cbranch_scc1 .LBB0_1594
	v_add_u32_e32 v2, s69, v220
	v_add_u32_e32 v2, 63, v2
	v_min_u32_e32 v222, 0x80, v2
	v_lshl_add_u32 v222, v222, 2, 0
	v_add_u32_e32 v222, 0x14c00, v222
	ds_read_b32 v68, v222
	v_med3_i32 v223, v2, 32, v214
	v_lshl_add_u32 v223, v223, 2, s16
	v_add_u32_e32 v223, 0xffffff80, v223
	ds_read_b32 v116, v223
	v_add_u32_e32 v221, -1, v2
	v_min_u32_e32 v222, 0x80, v221
	v_lshl_add_u32 v222, v222, 2, 0
	v_add_u32_e32 v222, 0x14c00, v222
	ds_read_b32 v69, v222
	v_med3_i32 v223, v221, 32, v214
	v_lshl_add_u32 v223, v223, 2, s16
	v_add_u32_e32 v223, 0xffffff80, v223
	ds_read_b32 v117, v223
	v_add_u32_e32 v221, -2, v2
	v_min_u32_e32 v222, 0x80, v221
	v_lshl_add_u32 v222, v222, 2, 0
	v_add_u32_e32 v222, 0x14c00, v222
	ds_read_b32 v70, v222
	v_med3_i32 v223, v221, 32, v214
	v_lshl_add_u32 v223, v223, 2, s16
	v_add_u32_e32 v223, 0xffffff80, v223
	ds_read_b32 v118, v223
	v_add_u32_e32 v221, -3, v2
	v_min_u32_e32 v222, 0x80, v221
	v_lshl_add_u32 v222, v222, 2, 0
	v_add_u32_e32 v222, 0x14c00, v222
	ds_read_b32 v71, v222
	v_med3_i32 v223, v221, 32, v214
	v_lshl_add_u32 v223, v223, 2, s16
	v_add_u32_e32 v223, 0xffffff80, v223
	ds_read_b32 v119, v223
	v_add_u32_e32 v221, -8, v2
	v_min_u32_e32 v222, 0x80, v221
	v_lshl_add_u32 v222, v222, 2, 0
	v_add_u32_e32 v222, 0x14c00, v222
	ds_read_b32 v72, v222
	v_med3_i32 v223, v221, 32, v214
	v_lshl_add_u32 v223, v223, 2, s16
	v_add_u32_e32 v223, 0xffffff80, v223
	ds_read_b32 v120, v223
	v_add_u32_e32 v221, -9, v2
	v_min_u32_e32 v222, 0x80, v221
	v_lshl_add_u32 v222, v222, 2, 0
	v_add_u32_e32 v222, 0x14c00, v222
	ds_read_b32 v73, v222
	v_med3_i32 v223, v221, 32, v214
	v_lshl_add_u32 v223, v223, 2, s16
	v_add_u32_e32 v223, 0xffffff80, v223
	ds_read_b32 v121, v223
	v_add_u32_e32 v221, -10, v2
	v_min_u32_e32 v222, 0x80, v221
	v_lshl_add_u32 v222, v222, 2, 0
	v_add_u32_e32 v222, 0x14c00, v222
	ds_read_b32 v74, v222
	v_med3_i32 v223, v221, 32, v214
	v_lshl_add_u32 v223, v223, 2, s16
	v_add_u32_e32 v223, 0xffffff80, v223
	ds_read_b32 v122, v223
	v_add_u32_e32 v221, -11, v2
	v_min_u32_e32 v222, 0x80, v221
	v_lshl_add_u32 v222, v222, 2, 0
	v_add_u32_e32 v222, 0x14c00, v222
	ds_read_b32 v75, v222
	v_med3_i32 v223, v221, 32, v214
	v_lshl_add_u32 v223, v223, 2, s16
	v_add_u32_e32 v223, 0xffffff80, v223
	ds_read_b32 v123, v223
	v_add_u32_e32 v221, -16, v2
	v_min_u32_e32 v222, 0x80, v221
	v_lshl_add_u32 v222, v222, 2, 0
	v_add_u32_e32 v222, 0x14c00, v222
	ds_read_b32 v76, v222
	v_med3_i32 v223, v221, 32, v214
	v_lshl_add_u32 v223, v223, 2, s16
	v_add_u32_e32 v223, 0xffffff80, v223
	ds_read_b32 v124, v223
	v_add_u32_e32 v221, 0xffffffef, v2
	v_min_u32_e32 v222, 0x80, v221
; #define SBAR() __builtin_amdgcn_sched_barrier(0)
; template <bool MLA>
; __device__ __forceinline__ void attn_unit(char* lds, int h, int qb, const bf16_t* Qp, int ldq, const bf16_t* Kp, int ldk, const bf16_t* KRp, const bf16_t* Vp, int ldv,
;                                           unsigned char* Op, int ldo, const float* KMp, const float* rel_bias) {
;     ...
;                 else {
; #pragma unroll
;                     for (int r4 = 0; r4 < 4; ++r4) {
; #pragma unroll
;                         for (int rr = 0; rr < 4; ++rr) { const int r = r4 * 4 + rr; const int d0 = dq - CROWC(r), d1 = d0 - 32;
;                             const float b0 = bt_l[d0 < 0 ? 0 : (d0 > 128 ? 128 : d0)], b1 = bt_l[d1 < 0 ? 0 : (d1 > 128 ? 128 : d1)];
;                             p0[r] = (selq && d0 >= 0) ? p0[r] + b0 : NEG; p1[r] = (selq && d1 >= 0) ? p1[r] + b1 : NEG; }
;                         SBAR(); } }
	v_lshl_add_u32 v222, v222, 2, 0
	v_add_u32_e32 v222, 0x14c00, v222
	ds_read_b32 v77, v222
	v_med3_i32 v223, v221, 32, v214
	v_lshl_add_u32 v223, v223, 2, s16
	v_add_u32_e32 v223, 0xffffff80, v223
	ds_read_b32 v125, v223
	v_add_u32_e32 v221, 0xffffffee, v2
	v_min_u32_e32 v222, 0x80, v221
	v_lshl_add_u32 v222, v222, 2, 0
	v_add_u32_e32 v222, 0x14c00, v222
	ds_read_b32 v78, v222
	v_med3_i32 v223, v221, 32, v214
	v_lshl_add_u32 v223, v223, 2, s16
	v_add_u32_e32 v223, 0xffffff80, v223
	ds_read_b32 v126, v223
	v_add_u32_e32 v221, 0xffffffed, v2
	v_min_u32_e32 v222, 0x80, v221
	v_lshl_add_u32 v222, v222, 2, 0
	v_add_u32_e32 v222, 0x14c00, v222
	ds_read_b32 v79, v222
	v_med3_i32 v223, v221, 32, v214
	v_lshl_add_u32 v223, v223, 2, s16
	v_add_u32_e32 v223, 0xffffff80, v223
	ds_read_b32 v127, v223
	v_add_u32_e32 v221, 0xffffffe8, v2
	v_min_u32_e32 v222, 0x80, v221
	v_lshl_add_u32 v222, v222, 2, 0
	v_add_u32_e32 v222, 0x14c00, v222
	ds_read_b32 v80, v222
	v_med3_i32 v223, v221, 32, v214
	v_lshl_add_u32 v223, v223, 2, s16
	v_add_u32_e32 v223, 0xffffff80, v223
	ds_read_b32 v128, v223
	v_add_u32_e32 v221, 0xffffffe7, v2
	v_min_u32_e32 v222, 0x80, v221
	v_lshl_add_u32 v222, v222, 2, 0
	v_add_u32_e32 v222, 0x14c00, v222
	ds_read_b32 v81, v222
	v_med3_i32 v223, v221, 32, v214
	v_lshl_add_u32 v223, v223, 2, s16
	v_add_u32_e32 v223, 0xffffff80, v223
	ds_read_b32 v129, v223
	v_add_u32_e32 v221, 0xffffffe6, v2
	v_min_u32_e32 v222, 0x80, v221
	v_lshl_add_u32 v222, v222, 2, 0
	v_add_u32_e32 v222, 0x14c00, v222
	ds_read_b32 v82, v222
	v_med3_i32 v223, v221, 32, v214
	v_lshl_add_u32 v223, v223, 2, s16
	v_add_u32_e32 v223, 0xffffff80, v223
	ds_read_b32 v130, v223
	v_add_u32_e32 v221, 0xffffffe5, v2
	v_min_u32_e32 v222, 0x80, v221
	v_lshl_add_u32 v222, v222, 2, 0
	v_add_u32_e32 v222, 0x14c00, v222
	ds_read_b32 v83, v222
	v_med3_i32 v223, v221, 32, v214
	v_lshl_add_u32 v223, v223, 2, s16
	v_add_u32_e32 v223, 0xffffff80, v223
	ds_read_b32 v131, v223
	s_waitcnt lgkmcnt(0)
	v_cmp_lt_i32_e32 vcc, -1, v2
	v_add_f32_e32 v68, v100, v68
	s_and_b64 vcc, vcc, s[12:13]
	v_cndmask_b32_e32 v68, v215, v68, vcc
	v_cmp_lt_i32_e32 vcc, 31, v2
	v_add_f32_e32 v116, v84, v116
	s_and_b64 vcc, vcc, s[12:13]
	v_cndmask_b32_e32 v116, v215, v116, vcc
	v_add_u32_e32 v221, -1, v2
	v_cmp_lt_i32_e32 vcc, -1, v221
	v_add_f32_e32 v69, v101, v69
	s_and_b64 vcc, vcc, s[12:13]
	v_cndmask_b32_e32 v69, v215, v69, vcc
	v_cmp_lt_i32_e32 vcc, 31, v221
	v_add_f32_e32 v117, v85, v117
	s_and_b64 vcc, vcc, s[12:13]
	v_cndmask_b32_e32 v117, v215, v117, vcc
	v_add_u32_e32 v221, -2, v2
	v_cmp_lt_i32_e32 vcc, -1, v221
	v_add_f32_e32 v70, v102, v70
	s_and_b64 vcc, vcc, s[12:13]
	v_cndmask_b32_e32 v70, v215, v70, vcc
	v_cmp_lt_i32_e32 vcc, 31, v221
	v_add_f32_e32 v118, v86, v118
	s_and_b64 vcc, vcc, s[12:13]
	v_cndmask_b32_e32 v118, v215, v118, vcc
	v_add_u32_e32 v221, -3, v2
	v_cmp_lt_i32_e32 vcc, -1, v221
	v_add_f32_e32 v71, v103, v71
	s_and_b64 vcc, vcc, s[12:13]
	v_cndmask_b32_e32 v71, v215, v71, vcc
	v_cmp_lt_i32_e32 vcc, 31, v221
	v_add_f32_e32 v119, v87, v119
	s_and_b64 vcc, vcc, s[12:13]
	v_cndmask_b32_e32 v119, v215, v119, vcc
	v_add_u32_e32 v221, -8, v2
	v_cmp_lt_i32_e32 vcc, -1, v221
	v_add_f32_e32 v72, v104, v72
	s_and_b64 vcc, vcc, s[12:13]
	v_cndmask_b32_e32 v72, v215, v72, vcc
	v_cmp_lt_i32_e32 vcc, 31, v221
	v_add_f32_e32 v120, v88, v120
	s_and_b64 vcc, vcc, s[12:13]
	v_cndmask_b32_e32 v120, v215, v120, vcc
	v_add_u32_e32 v221, -9, v2
	v_cmp_lt_i32_e32 vcc, -1, v221
	v_add_f32_e32 v73, v105, v73
	s_and_b64 vcc, vcc, s[12:13]
	v_cndmask_b32_e32 v73, v215, v73, vcc
	v_cmp_lt_i32_e32 vcc, 31, v221
	v_add_f32_e32 v121, v89, v121
	s_and_b64 vcc, vcc, s[12:13]
	v_cndmask_b32_e32 v121, v215, v121, vcc
	v_add_u32_e32 v221, -10, v2
	v_cmp_lt_i32_e32 vcc, -1, v221
	v_add_f32_e32 v74, v106, v74
	s_and_b64 vcc, vcc, s[12:13]
	v_cndmask_b32_e32 v74, v215, v74, vcc
	v_cmp_lt_i32_e32 vcc, 31, v221
	v_add_f32_e32 v122, v90, v122
	s_and_b64 vcc, vcc, s[12:13]
	v_cndmask_b32_e32 v122, v215, v122, vcc
	v_add_u32_e32 v221, -11, v2
	v_cmp_lt_i32_e32 vcc, -1, v221
	v_add_f32_e32 v75, v107, v75
	s_and_b64 vcc, vcc, s[12:13]
	v_cndmask_b32_e32 v75, v215, v75, vcc
	v_cmp_lt_i32_e32 vcc, 31, v221
	v_add_f32_e32 v123, v91, v123
	s_and_b64 vcc, vcc, s[12:13]
	v_cndmask_b32_e32 v123, v215, v123, vcc
	v_add_u32_e32 v221, -16, v2
	v_cmp_lt_i32_e32 vcc, -1, v221
	v_add_f32_e32 v76, v108, v76
	s_and_b64 vcc, vcc, s[12:13]
	v_cndmask_b32_e32 v76, v215, v76, vcc
	v_cmp_lt_i32_e32 vcc, 31, v221
	v_add_f32_e32 v124, v92, v124
	s_and_b64 vcc, vcc, s[12:13]
	v_cndmask_b32_e32 v124, v215, v124, vcc
	v_add_u32_e32 v221, 0xffffffef, v2
	v_cmp_lt_i32_e32 vcc, -1, v221
	v_add_f32_e32 v77, v109, v77
	s_and_b64 vcc, vcc, s[12:13]
	v_cndmask_b32_e32 v77, v215, v77, vcc
	v_cmp_lt_i32_e32 vcc, 31, v221
	v_add_f32_e32 v125, v93, v125
	s_and_b64 vcc, vcc, s[12:13]
	v_cndmask_b32_e32 v125, v215, v125, vcc
	v_add_u32_e32 v221, 0xffffffee, v2
	v_cmp_lt_i32_e32 vcc, -1, v221
	v_add_f32_e32 v78, v110, v78
	s_and_b64 vcc, vcc, s[12:13]
	v_cndmask_b32_e32 v78, v215, v78, vcc
	v_cmp_lt_i32_e32 vcc, 31, v221
	v_add_f32_e32 v126, v94, v126
	s_and_b64 vcc, vcc, s[12:13]
	v_cndmask_b32_e32 v126, v215, v126, vcc
	v_add_u32_e32 v221, 0xffffffed, v2
	v_cmp_lt_i32_e32 vcc, -1, v221
	v_add_f32_e32 v79, v111, v79
	s_and_b64 vcc, vcc, s[12:13]
	v_cndmask_b32_e32 v79, v215, v79, vcc
	v_cmp_lt_i32_e32 vcc, 31, v221
	v_add_f32_e32 v127, v95, v127
	s_and_b64 vcc, vcc, s[12:13]
	v_cndmask_b32_e32 v127, v215, v127, vcc
	v_add_u32_e32 v221, 0xffffffe8, v2
	v_cmp_lt_i32_e32 vcc, -1, v221
	v_add_f32_e32 v80, v112, v80
	s_and_b64 vcc, vcc, s[12:13]
	v_cndmask_b32_e32 v80, v215, v80, vcc
	v_cmp_lt_i32_e32 vcc, 31, v221
	v_add_f32_e32 v128, v96, v128
	s_and_b64 vcc, vcc, s[12:13]
	v_cndmask_b32_e32 v128, v215, v128, vcc
	v_add_u32_e32 v221, 0xffffffe7, v2
	v_cmp_lt_i32_e32 vcc, -1, v221
	v_add_f32_e32 v81, v113, v81
	s_and_b64 vcc, vcc, s[12:13]
	v_cndmask_b32_e32 v81, v215, v81, vcc
	v_cmp_lt_i32_e32 vcc, 31, v221
	v_add_f32_e32 v129, v97, v129
	s_and_b64 vcc, vcc, s[12:13]
	v_cndmask_b32_e32 v129, v215, v129, vcc
	v_add_u32_e32 v221, 0xffffffe6, v2
	v_cmp_lt_i32_e32 vcc, -1, v221
	v_add_f32_e32 v82, v114, v82
	s_and_b64 vcc, vcc, s[12:13]
	v_cndmask_b32_e32 v82, v215, v82, vcc
	v_cmp_lt_i32_e32 vcc, 31, v221
	v_add_f32_e32 v130, v98, v130
	s_and_b64 vcc, vcc, s[12:13]
	v_cndmask_b32_e32 v130, v215, v130, vcc
	v_add_u32_e32 v221, 0xffffffe5, v2
	v_cmp_lt_i32_e32 vcc, -1, v221
	v_add_f32_e32 v83, v115, v83
	s_and_b64 vcc, vcc, s[12:13]
	v_cndmask_b32_e32 v83, v215, v83, vcc
	v_cmp_lt_i32_e32 vcc, 31, v221
	v_add_f32_e32 v131, v99, v131
	s_and_b64 vcc, vcc, s[12:13]
	v_cndmask_b32_e32 v131, v215, v131, vcc
	s_mov_b64 s[54:55], 0

; template <bool MLA>
; __device__ __forceinline__ void attn_unit(char* lds, int h, int qb, const bf16_t* Qp, int ldq, const bf16_t* Kp, int ldk, const bf16_t* KRp, const bf16_t* Vp, int ldv,
;                                           unsigned char* Op, int ldo, const float* KMp, const float* rel_bias) {
;     ...
;             { const char* kn = lds + buf * SHM_KN; const char* kr = lds + buf * SHM_KR;
; #pragma unroll
;               for (int d0 = 0; d0 < 8; ++d0) { const char* ap = kn + kan[d0 & 3] + (d0 >> 2) * 128;
;                   const bf16x8 a0 = *(const bf16x8*)ap, a1 = *(const bf16x8*)(ap + 32 * 256);
;                   p0 = __builtin_amdgcn_mfma_f32_32x32x16_bf16(a0, qr[d0], p0, 0, 0, 0);
;                   p1 = __builtin_amdgcn_mfma_f32_32x32x16_bf16(a1, qr[d0], p1, 0, 0, 0); }
;               if constexpr (MLA) {
; #pragma unroll
;                   for (int d0 = 8; d0 < 12; ++d0) { const char* ap = kr + kar[d0 & 3];
;                       const bf16x8 a0 = *(const bf16x8*)ap, a1 = *(const bf16x8*)(ap + 32 * 128);
;                       p0 = __builtin_amdgcn_mfma_f32_32x32x16_bf16(a0, qr[d0], p0, 0, 0, 0);
;                       p1 = __builtin_amdgcn_mfma_f32_32x32x16_bf16(a1, qr[d0], p1, 0, 0, 0); } } }
;             const int dq = qpos - kb - 4 * hi;
;             if constexpr (MLA) {
;                 if (kb + 63 > qlo) {
; #pragma unroll
;                     for (int r = 0; r < 16; ++r) { const int d0 = dq - CROWC(r); if (d0 < 0) p0[r] = NEG; if (d0 < 32) p1[r] = NEG; } }
;             } else {
;                 const bool selq = (jb == qb) || (((mysel >> jb) & 1u) != 0u);
;                 if (q0 - (kb + 63) >= 128) { const float cb = bt_l[128];
; #pragma unroll
;                     for (int r = 0; r < 16; ++r) { p0[r] = selq ? p0[r] + cb : NEG; p1[r] = selq ? p1[r] + cb : NEG; } }
;                 else {
; #pragma unroll
;                     for (int r4 = 0; r4 < 4; ++r4) {
; #pragma unroll
;                         for (int rr = 0; rr < 4; ++rr) { const int r = r4 * 4 + rr; const int d0 = dq - CROWC(r), d1 = d0 - 32;
;                             const float b0 = bt_l[d0 < 0 ? 0 : (d0 > 128 ? 128 : d0)], b1 = bt_l[d1 < 0 ? 0 : (d1 > 128 ? 128 : d1)];
;                             p0[r] = (selq && d0 >= 0) ? p0[r] + b0 : NEG; p1[r] = (selq && d1 >= 0) ? p1[r] + b1 : NEG; }
;                         SBAR(); } }
.LBB0_1603:
	v_cndmask_b32_e64 v2, 0, 1, s[52:53]
	s_nop 0
	v_readfirstlane_b32 s22, v2
	s_bitcmp0_b32 s22, 0
	s_cbranch_scc1 .LBB0_1645
	s_lshl_b32 s22, s66, 14
	s_and_b32 s26, s22, 0x4000
	s_add_i32 s22, s26, 0
	v_add_u32_e32 v2, s22, v203
	ds_read_b128 v[68:71], v2 offset:32768
	ds_read_b128 v[72:75], v2 offset:32896
	s_mov_b64 s[52:53], -1
	s_waitcnt lgkmcnt(1)
	v_mfma_f32_32x32x16_bf16 v[100:115], v[68:71], v[160:163], 0
	ds_read_b128 v[68:71], v2 offset:40960
	ds_read_b128 v[76:79], v2 offset:41088
	v_add_u32_e32 v2, s22, v204
	s_waitcnt lgkmcnt(1)
	v_mfma_f32_32x32x16_bf16 v[84:99], v[68:71], v[160:163], 0
	ds_read_b128 v[68:71], v2 offset:32768
	ds_read_b128 v[80:83], v2 offset:32896
	s_waitcnt lgkmcnt(1)
	v_mfma_f32_32x32x16_bf16 v[100:115], v[68:71], v[156:159], v[100:115]
	ds_read_b128 v[68:71], v2 offset:40960
	ds_read_b128 v[116:119], v2 offset:41088
	v_add_u32_e32 v2, s22, v205
	s_waitcnt lgkmcnt(1)
	v_mfma_f32_32x32x16_bf16 v[84:99], v[68:71], v[156:159], v[84:99]
	ds_read_b128 v[68:71], v2 offset:32768
	ds_read_b128 v[120:123], v2 offset:32896
	s_waitcnt lgkmcnt(1)
	v_mfma_f32_32x32x16_bf16 v[100:115], v[68:71], v[152:155], v[100:115]
	ds_read_b128 v[68:71], v2 offset:40960
	ds_read_b128 v[124:127], v2 offset:41088
	v_add_u32_e32 v2, s22, v206
	s_lshl_b32 s22, 1, s27
	s_waitcnt lgkmcnt(1)
	v_mfma_f32_32x32x16_bf16 v[84:99], v[68:71], v[152:155], v[84:99]
	ds_read_b128 v[68:71], v2 offset:32768
	ds_read_b128 v[128:131], v2 offset:32896
	s_waitcnt lgkmcnt(1)
	v_mfma_f32_32x32x16_bf16 v[100:115], v[68:71], v[148:151], v[100:115]
	ds_read_b128 v[68:71], v2 offset:40960
	ds_read_b128 v[152:155], v2 offset:41088
	v_and_b32_e32 v2, s22, v219
	v_cmp_ne_u32_e32 vcc, 0, v2
	s_or_b64 s[12:13], s[12:13], vcc
	s_sub_i32 s22, s65, s54
	s_cmpk_gt_i32 s22, 0x7f
	s_waitcnt lgkmcnt(1)
	v_mfma_f32_32x32x16_bf16 v[84:99], v[68:71], v[148:151], v[84:99]
	v_mfma_f32_32x32x16_bf16 v[100:115], v[72:75], v[144:147], v[100:115]
	v_mfma_f32_32x32x16_bf16 v[84:99], v[76:79], v[144:147], v[84:99]
	v_mfma_f32_32x32x16_bf16 v[100:115], v[80:83], v[140:143], v[100:115]
	v_mfma_f32_32x32x16_bf16 v[84:99], v[116:119], v[140:143], v[84:99]
	v_mfma_f32_32x32x16_bf16 v[100:115], v[120:123], v[136:139], v[100:115]
	v_mfma_f32_32x32x16_bf16 v[84:99], v[124:127], v[136:139], v[84:99]
	v_mfma_f32_32x32x16_bf16 v[100:115], v[128:131], v[132:135], v[100:115]
	s_waitcnt lgkmcnt(0)
	v_mfma_f32_32x32x16_bf16 v[84:99], v[152:155], v[132:135], v[84:99]
	s_cbranch_scc1 .LBB0_1638
	v_subrev_u32_e32 v2, s54, v218
	v_sub_u32_e32 v2, v2, v165
	v_min_u32_e32 v133, 0x80, v2
	v_lshl_add_u32 v133, v133, 2, 0
	v_add_u32_e32 v133, 0x14c00, v133
	ds_read_b32 v68, v133
	v_med3_i32 v134, v2, 32, v214
	v_lshl_add_u32 v134, v134, 2, s16
	v_add_u32_e32 v134, 0xffffff80, v134
	ds_read_b32 v116, v134
	v_add_u32_e32 v132, -1, v2
	v_min_u32_e32 v133, 0x80, v132
	v_lshl_add_u32 v133, v133, 2, 0
	v_add_u32_e32 v133, 0x14c00, v133
	ds_read_b32 v69, v133
	v_med3_i32 v134, v132, 32, v214
	v_lshl_add_u32 v134, v134, 2, s16
	v_add_u32_e32 v134, 0xffffff80, v134
	ds_read_b32 v117, v134
	v_add_u32_e32 v132, -2, v2
	v_min_u32_e32 v133, 0x80, v132
	v_lshl_add_u32 v133, v133, 2, 0
	v_add_u32_e32 v133, 0x14c00, v133
	ds_read_b32 v70, v133
	v_med3_i32 v134, v132, 32, v214
	v_lshl_add_u32 v134, v134, 2, s16
	v_add_u32_e32 v134, 0xffffff80, v134
	ds_read_b32 v118, v134
	v_add_u32_e32 v132, -3, v2
	v_min_u32_e32 v133, 0x80, v132
	v_lshl_add_u32 v133, v133, 2, 0
	v_add_u32_e32 v133, 0x14c00, v133
	ds_read_b32 v71, v133
	v_med3_i32 v134, v132, 32, v214
	v_lshl_add_u32 v134, v134, 2, s16
	v_add_u32_e32 v134, 0xffffff80, v134
	ds_read_b32 v119, v134
	v_add_u32_e32 v132, -8, v2
	v_min_u32_e32 v133, 0x80, v132
	v_lshl_add_u32 v133, v133, 2, 0
	v_add_u32_e32 v133, 0x14c00, v133
	ds_read_b32 v72, v133
	v_med3_i32 v134, v132, 32, v214
	v_lshl_add_u32 v134, v134, 2, s16
	v_add_u32_e32 v134, 0xffffff80, v134
	ds_read_b32 v120, v134
	v_add_u32_e32 v132, -9, v2
	v_min_u32_e32 v133, 0x80, v132
	v_lshl_add_u32 v133, v133, 2, 0
	v_add_u32_e32 v133, 0x14c00, v133
	ds_read_b32 v73, v133
	v_med3_i32 v134, v132, 32, v214
	v_lshl_add_u32 v134, v134, 2, s16
	v_add_u32_e32 v134, 0xffffff80, v134
	ds_read_b32 v121, v134
	v_add_u32_e32 v132, -10, v2
	v_min_u32_e32 v133, 0x80, v132
	v_lshl_add_u32 v133, v133, 2, 0
	v_add_u32_e32 v133, 0x14c00, v133
	ds_read_b32 v74, v133
	v_med3_i32 v134, v132, 32, v214
	v_lshl_add_u32 v134, v134, 2, s16
	v_add_u32_e32 v134, 0xffffff80, v134
	ds_read_b32 v122, v134
	v_add_u32_e32 v132, -11, v2
	v_min_u32_e32 v133, 0x80, v132
	v_lshl_add_u32 v133, v133, 2, 0
	v_add_u32_e32 v133, 0x14c00, v133
	ds_read_b32 v75, v133
	v_med3_i32 v134, v132, 32, v214
	v_lshl_add_u32 v134, v134, 2, s16
	v_add_u32_e32 v134, 0xffffff80, v134
	ds_read_b32 v123, v134
	v_add_u32_e32 v132, -16, v2
	v_min_u32_e32 v133, 0x80, v132
	v_lshl_add_u32 v133, v133, 2, 0
	v_add_u32_e32 v133, 0x14c00, v133
	ds_read_b32 v76, v133
	v_med3_i32 v134, v132, 32, v214
	v_lshl_add_u32 v134, v134, 2, s16
	v_add_u32_e32 v134, 0xffffff80, v134
	ds_read_b32 v124, v134
	v_add_u32_e32 v132, 0xffffffef, v2
	v_min_u32_e32 v133, 0x80, v132
	v_lshl_add_u32 v133, v133, 2, 0
	v_add_u32_e32 v133, 0x14c00, v133
	ds_read_b32 v77, v133
	v_med3_i32 v134, v132, 32, v214
	v_lshl_add_u32 v134, v134, 2, s16
	v_add_u32_e32 v134, 0xffffff80, v134
	ds_read_b32 v125, v134
	v_add_u32_e32 v132, 0xffffffee, v2
	v_min_u32_e32 v133, 0x80, v132
	v_lshl_add_u32 v133, v133, 2, 0
	v_add_u32_e32 v133, 0x14c00, v133
	ds_read_b32 v78, v133
	v_med3_i32 v134, v132, 32, v214
	v_lshl_add_u32 v134, v134, 2, s16
	v_add_u32_e32 v134, 0xffffff80, v134
	ds_read_b32 v126, v134
; #define SBAR() __builtin_amdgcn_sched_barrier(0)
; template <bool MLA>
; __device__ __forceinline__ void attn_unit(char* lds, int h, int qb, const bf16_t* Qp, int ldq, const bf16_t* Kp, int ldk, const bf16_t* KRp, const bf16_t* Vp, int ldv,
;                                           unsigned char* Op, int ldo, const float* KMp, const float* rel_bias) {
;     ...
;                 else {
; #pragma unroll
;                     for (int r4 = 0; r4 < 4; ++r4) {
; #pragma unroll
;                         for (int rr = 0; rr < 4; ++rr) { const int r = r4 * 4 + rr; const int d0 = dq - CROWC(r), d1 = d0 - 32;
;                             const float b0 = bt_l[d0 < 0 ? 0 : (d0 > 128 ? 128 : d0)], b1 = bt_l[d1 < 0 ? 0 : (d1 > 128 ? 128 : d1)];
;                             p0[r] = (selq && d0 >= 0) ? p0[r] + b0 : NEG; p1[r] = (selq && d1 >= 0) ? p1[r] + b1 : NEG; }
;                         SBAR(); } }
	v_add_u32_e32 v132, 0xffffffed, v2
	v_min_u32_e32 v133, 0x80, v132
	v_lshl_add_u32 v133, v133, 2, 0
	v_add_u32_e32 v133, 0x14c00, v133
	ds_read_b32 v79, v133
	v_med3_i32 v134, v132, 32, v214
	v_lshl_add_u32 v134, v134, 2, s16
	v_add_u32_e32 v134, 0xffffff80, v134
	ds_read_b32 v127, v134
	v_add_u32_e32 v132, 0xffffffe8, v2
	v_min_u32_e32 v133, 0x80, v132
	v_lshl_add_u32 v133, v133, 2, 0
	v_add_u32_e32 v133, 0x14c00, v133
	ds_read_b32 v80, v133
	v_med3_i32 v134, v132, 32, v214
	v_lshl_add_u32 v134, v134, 2, s16
	v_add_u32_e32 v134, 0xffffff80, v134
	ds_read_b32 v128, v134
	v_add_u32_e32 v132, 0xffffffe7, v2
	v_min_u32_e32 v133, 0x80, v132
	v_lshl_add_u32 v133, v133, 2, 0
	v_add_u32_e32 v133, 0x14c00, v133
	ds_read_b32 v81, v133
	v_med3_i32 v134, v132, 32, v214
	v_lshl_add_u32 v134, v134, 2, s16
	v_add_u32_e32 v134, 0xffffff80, v134
	ds_read_b32 v129, v134
	v_add_u32_e32 v132, 0xffffffe6, v2
	v_min_u32_e32 v133, 0x80, v132
	v_lshl_add_u32 v133, v133, 2, 0
	v_add_u32_e32 v133, 0x14c00, v133
	ds_read_b32 v82, v133
	v_med3_i32 v134, v132, 32, v214
	v_lshl_add_u32 v134, v134, 2, s16
	v_add_u32_e32 v134, 0xffffff80, v134
	ds_read_b32 v130, v134
	v_add_u32_e32 v132, 0xffffffe5, v2
	v_min_u32_e32 v133, 0x80, v132
	v_lshl_add_u32 v133, v133, 2, 0
	v_add_u32_e32 v133, 0x14c00, v133
	ds_read_b32 v83, v133
	v_med3_i32 v134, v132, 32, v214
	v_lshl_add_u32 v134, v134, 2, s16
	v_add_u32_e32 v134, 0xffffff80, v134
	ds_read_b32 v131, v134
	s_waitcnt lgkmcnt(0)
	v_cmp_lt_i32_e32 vcc, -1, v2
	v_add_f32_e32 v68, v100, v68
	s_and_b64 vcc, vcc, s[12:13]
	v_cndmask_b32_e32 v68, v215, v68, vcc
	v_cmp_lt_i32_e32 vcc, 31, v2
	v_add_f32_e32 v116, v84, v116
	s_and_b64 vcc, vcc, s[12:13]
	v_cndmask_b32_e32 v116, v215, v116, vcc
	v_add_u32_e32 v132, -1, v2
	v_cmp_lt_i32_e32 vcc, -1, v132
	v_add_f32_e32 v69, v101, v69
	s_and_b64 vcc, vcc, s[12:13]
	v_cndmask_b32_e32 v69, v215, v69, vcc
	v_cmp_lt_i32_e32 vcc, 31, v132
	v_add_f32_e32 v117, v85, v117
	s_and_b64 vcc, vcc, s[12:13]
	v_cndmask_b32_e32 v117, v215, v117, vcc
	v_add_u32_e32 v132, -2, v2
	v_cmp_lt_i32_e32 vcc, -1, v132
	v_add_f32_e32 v70, v102, v70
	s_and_b64 vcc, vcc, s[12:13]
	v_cndmask_b32_e32 v70, v215, v70, vcc
	v_cmp_lt_i32_e32 vcc, 31, v132
	v_add_f32_e32 v118, v86, v118
	s_and_b64 vcc, vcc, s[12:13]
	v_cndmask_b32_e32 v118, v215, v118, vcc
	v_add_u32_e32 v132, -3, v2
	v_cmp_lt_i32_e32 vcc, -1, v132
	v_add_f32_e32 v71, v103, v71
	s_and_b64 vcc, vcc, s[12:13]
	v_cndmask_b32_e32 v71, v215, v71, vcc
	v_cmp_lt_i32_e32 vcc, 31, v132
	v_add_f32_e32 v119, v87, v119
	s_and_b64 vcc, vcc, s[12:13]
	v_cndmask_b32_e32 v119, v215, v119, vcc
	v_add_u32_e32 v132, -8, v2
	v_cmp_lt_i32_e32 vcc, -1, v132
	v_add_f32_e32 v72, v104, v72
	s_and_b64 vcc, vcc, s[12:13]
	v_cndmask_b32_e32 v72, v215, v72, vcc
	v_cmp_lt_i32_e32 vcc, 31, v132
	v_add_f32_e32 v120, v88, v120
	s_and_b64 vcc, vcc, s[12:13]
	v_cndmask_b32_e32 v120, v215, v120, vcc
	v_add_u32_e32 v132, -9, v2
	v_cmp_lt_i32_e32 vcc, -1, v132
	v_add_f32_e32 v73, v105, v73
	s_and_b64 vcc, vcc, s[12:13]
	v_cndmask_b32_e32 v73, v215, v73, vcc
	v_cmp_lt_i32_e32 vcc, 31, v132
	v_add_f32_e32 v121, v89, v121
	s_and_b64 vcc, vcc, s[12:13]
	v_cndmask_b32_e32 v121, v215, v121, vcc
	v_add_u32_e32 v132, -10, v2
	v_cmp_lt_i32_e32 vcc, -1, v132
	v_add_f32_e32 v74, v106, v74
	s_and_b64 vcc, vcc, s[12:13]
	v_cndmask_b32_e32 v74, v215, v74, vcc
	v_cmp_lt_i32_e32 vcc, 31, v132
	v_add_f32_e32 v122, v90, v122
	s_and_b64 vcc, vcc, s[12:13]
	v_cndmask_b32_e32 v122, v215, v122, vcc
	v_add_u32_e32 v132, -11, v2
	v_cmp_lt_i32_e32 vcc, -1, v132
	v_add_f32_e32 v75, v107, v75
	s_and_b64 vcc, vcc, s[12:13]
	v_cndmask_b32_e32 v75, v215, v75, vcc
	v_cmp_lt_i32_e32 vcc, 31, v132
	v_add_f32_e32 v123, v91, v123
	s_and_b64 vcc, vcc, s[12:13]
	v_cndmask_b32_e32 v123, v215, v123, vcc
	v_add_u32_e32 v132, -16, v2
	v_cmp_lt_i32_e32 vcc, -1, v132
	v_add_f32_e32 v76, v108, v76
	s_and_b64 vcc, vcc, s[12:13]
	v_cndmask_b32_e32 v76, v215, v76, vcc
	v_cmp_lt_i32_e32 vcc, 31, v132
	v_add_f32_e32 v124, v92, v124
	s_and_b64 vcc, vcc, s[12:13]
	v_cndmask_b32_e32 v124, v215, v124, vcc
	v_add_u32_e32 v132, 0xffffffef, v2
	v_cmp_lt_i32_e32 vcc, -1, v132
	v_add_f32_e32 v77, v109, v77
	s_and_b64 vcc, vcc, s[12:13]
	v_cndmask_b32_e32 v77, v215, v77, vcc
	v_cmp_lt_i32_e32 vcc, 31, v132
	v_add_f32_e32 v125, v93, v125
	s_and_b64 vcc, vcc, s[12:13]
	v_cndmask_b32_e32 v125, v215, v125, vcc
	v_add_u32_e32 v132, 0xffffffee, v2
	v_cmp_lt_i32_e32 vcc, -1, v132
	v_add_f32_e32 v78, v110, v78
	s_and_b64 vcc, vcc, s[12:13]
	v_cndmask_b32_e32 v78, v215, v78, vcc
	v_cmp_lt_i32_e32 vcc, 31, v132
	v_add_f32_e32 v126, v94, v126
	s_and_b64 vcc, vcc, s[12:13]
	v_cndmask_b32_e32 v126, v215, v126, vcc
	v_add_u32_e32 v132, 0xffffffed, v2
	v_cmp_lt_i32_e32 vcc, -1, v132
	v_add_f32_e32 v79, v111, v79
	s_and_b64 vcc, vcc, s[12:13]
	v_cndmask_b32_e32 v79, v215, v79, vcc
	v_cmp_lt_i32_e32 vcc, 31, v132
	v_add_f32_e32 v127, v95, v127
	s_and_b64 vcc, vcc, s[12:13]
	v_cndmask_b32_e32 v127, v215, v127, vcc
	v_add_u32_e32 v132, 0xffffffe8, v2
	v_cmp_lt_i32_e32 vcc, -1, v132
	v_add_f32_e32 v80, v112, v80
	s_and_b64 vcc, vcc, s[12:13]
	v_cndmask_b32_e32 v80, v215, v80, vcc
	v_cmp_lt_i32_e32 vcc, 31, v132
	v_add_f32_e32 v128, v96, v128
	s_and_b64 vcc, vcc, s[12:13]
	v_cndmask_b32_e32 v128, v215, v128, vcc
	v_add_u32_e32 v132, 0xffffffe7, v2
	v_cmp_lt_i32_e32 vcc, -1, v132
	v_add_f32_e32 v81, v113, v81
	s_and_b64 vcc, vcc, s[12:13]
	v_cndmask_b32_e32 v81, v215, v81, vcc
	v_cmp_lt_i32_e32 vcc, 31, v132
	v_add_f32_e32 v129, v97, v129
	s_and_b64 vcc, vcc, s[12:13]
	v_cndmask_b32_e32 v129, v215, v129, vcc
	v_add_u32_e32 v132, 0xffffffe6, v2
	v_cmp_lt_i32_e32 vcc, -1, v132
	v_add_f32_e32 v82, v114, v82
	s_and_b64 vcc, vcc, s[12:13]
	v_cndmask_b32_e32 v82, v215, v82, vcc
	v_cmp_lt_i32_e32 vcc, 31, v132
	v_add_f32_e32 v130, v98, v130
	s_and_b64 vcc, vcc, s[12:13]
	v_cndmask_b32_e32 v130, v215, v130, vcc
	v_add_u32_e32 v132, 0xffffffe5, v2
	v_cmp_lt_i32_e32 vcc, -1, v132
	v_add_f32_e32 v83, v115, v83
	s_and_b64 vcc, vcc, s[12:13]
	v_cndmask_b32_e32 v83, v215, v83, vcc
	v_cmp_lt_i32_e32 vcc, 31, v132
	v_add_f32_e32 v131, v99, v131
	s_and_b64 vcc, vcc, s[12:13]
	v_cndmask_b32_e32 v131, v215, v131, vcc
	s_mov_b64 s[52:53], 0
